# norm2 prologue: eight router-weight loads per thread issued together (was one round trip each); plus the top-k latent unit edits
# speedup vs baseline: 1.0063x; 1.0006x over previous
.LBB0_1236:
	v_ashrrev_i32_e32 v6, 2, v3
	v_lshlrev_b32_e32 v7, 8, v6
	v_and_b32_e32 v7, 0x300, v7
	v_lshrrev_b32_e32 v8, 4, v3
	v_add_u32_e32 v10, v7, v8
	v_ashrrev_i32_e32 v7, 31, v6
	v_lshlrev_b64 v[6:7], 6, v[6:7]
	v_lshl_add_u64 v[6:7], v[4:5], 0, v[6:7]
	s_movk_i32 s1, 0x50
	v_mad_u64_u32 v[10:11], s[8:9], v10, s1, v[2:3]
	s_nop 1
	s_mov_b64 s[8:9], 0x2000
	global_load_dwordx4 v[20:23], v[6:7], off
	v_lshl_add_u64 v[6:7], v[6:7], 0, s[8:9]
	global_load_dwordx4 v[24:27], v[6:7], off
	v_lshl_add_u64 v[6:7], v[6:7], 0, s[8:9]
	global_load_dwordx4 v[28:31], v[6:7], off
	v_lshl_add_u64 v[6:7], v[6:7], 0, s[8:9]
	global_load_dwordx4 v[32:35], v[6:7], off
	v_lshl_add_u64 v[6:7], v[6:7], 0, s[8:9]
	global_load_dwordx4 v[36:39], v[6:7], off
	v_lshl_add_u64 v[6:7], v[6:7], 0, s[8:9]
	global_load_dwordx4 v[40:43], v[6:7], off
	v_lshl_add_u64 v[6:7], v[6:7], 0, s[8:9]
	global_load_dwordx4 v[44:47], v[6:7], off
	v_lshl_add_u64 v[6:7], v[6:7], 0, s[8:9]
	global_load_dwordx4 v[48:51], v[6:7], off
	s_waitcnt vmcnt(7)
	ds_write_b128 v10, v[20:23]
	s_waitcnt vmcnt(6)
	ds_write_b128 v10, v[24:27] offset:2560
	s_waitcnt vmcnt(5)
	ds_write_b128 v10, v[28:31] offset:5120
	s_waitcnt vmcnt(4)
	ds_write_b128 v10, v[32:35] offset:7680
	s_waitcnt vmcnt(3)
	ds_write_b128 v10, v[36:39] offset:10240
	s_waitcnt vmcnt(2)
	ds_write_b128 v10, v[40:43] offset:12800
	s_waitcnt vmcnt(1)
	ds_write_b128 v10, v[44:47] offset:15360
	s_waitcnt vmcnt(0)
	ds_write_b128 v10, v[48:51] offset:17920
